# speedup vs baseline: 1.0117x; 1.0117x over previous
_Z6gat_k2PKDF16_S0_S0_PKfPf:
	s_load_dwordx8 s[4:11], s[0:1], 0x0
	s_load_dwordx2 s[12:13], s[0:1], 0x20
	v_readfirstlane_b32 s14, v0
	v_and_b32_e32 v46, 63, v0
	v_lshlrev_b32_e32 v1, 4, v46
	s_and_b32 s16, s2, 1
	s_bfe_u32 s17, s2, 0x60003
	s_lshr_b32 s18, s2, 1
	s_lshr_b32 s15, s14, 6
	s_lshl_b32 s19, s16, 19
	s_lshl_b32 s23, s15, 16
	s_add_u32 s19, s19, s23
	s_lshl_b32 s23, s15, 11
	v_add_u32_e32 v47, s23, v1
	v_and_b32_e32 v44, 31, v0
	v_lshlrev_b32_e32 v45, 2, v44
	s_lshl_b32 s23, s18, 8
	v_add_u32_e32 v45, s23, v45
	s_waitcnt lgkmcnt(0)
	global_load_dword v42, v45, s[10:11]
	global_load_dword v43, v45, s[10:11] offset:128
	global_load_dwordx4 v[48:51], v47, s[6:7]
	global_load_dwordx4 v[52:55], v47, s[6:7] offset:1024
	global_load_dwordx4 v[56:59], v47, s[8:9]
	global_load_dwordx4 v[60:63], v47, s[8:9] offset:1024
	s_add_u32 s20, s4, s19
	s_addc_u32 s21, s5, 0
	s_add_u32 s23, s17, 0
	s_and_b32 s23, s23, 63
	s_lshl_b32 s23, s23, 10
	s_add_u32 s24, s20, s23
	s_addc_u32 s25, s21, 0
	global_load_dwordx4 v[64:67], v1, s[24:25]
	s_add_u32 s23, s17, 1
	s_and_b32 s23, s23, 63
	s_lshl_b32 s23, s23, 10
	s_add_u32 s24, s20, s23
	s_addc_u32 s25, s21, 0
	global_load_dwordx4 v[68:71], v1, s[24:25]
	s_add_u32 s23, s17, 2
	s_and_b32 s23, s23, 63
	s_lshl_b32 s23, s23, 10
	s_add_u32 s24, s20, s23
	s_addc_u32 s25, s21, 0
	global_load_dwordx4 v[72:75], v1, s[24:25]
	s_add_u32 s23, s17, 3
	s_and_b32 s23, s23, 63
	s_lshl_b32 s23, s23, 10
	s_add_u32 s24, s20, s23
	s_addc_u32 s25, s21, 0
	global_load_dwordx4 v[76:79], v1, s[24:25]
	s_add_u32 s23, s17, 4
	s_and_b32 s23, s23, 63
	s_lshl_b32 s23, s23, 10
	s_add_u32 s24, s20, s23
	s_addc_u32 s25, s21, 0
	global_load_dwordx4 v[80:83], v1, s[24:25]
	s_add_u32 s23, s17, 5
	s_and_b32 s23, s23, 63
	s_lshl_b32 s23, s23, 10
	s_add_u32 s24, s20, s23
	s_addc_u32 s25, s21, 0
	global_load_dwordx4 v[84:87], v1, s[24:25]
	s_add_u32 s23, s17, 6
	s_and_b32 s23, s23, 63
	s_lshl_b32 s23, s23, 10
	s_add_u32 s24, s20, s23
	s_addc_u32 s25, s21, 0
	global_load_dwordx4 v[88:91], v1, s[24:25]
	s_add_u32 s23, s17, 7
	s_and_b32 s23, s23, 63
	s_lshl_b32 s23, s23, 10
	s_add_u32 s24, s20, s23
	s_addc_u32 s25, s21, 0
	global_load_dwordx4 v[92:95], v1, s[24:25]
	v_accvgpr_write_b32 a0, 0
	v_accvgpr_write_b32 a1, 0
	v_accvgpr_write_b32 a2, 0
	v_accvgpr_write_b32 a3, 0
	v_accvgpr_write_b32 a4, 0
	v_accvgpr_write_b32 a5, 0
	v_accvgpr_write_b32 a6, 0
	v_accvgpr_write_b32 a7, 0
	v_accvgpr_write_b32 a8, 0
	v_accvgpr_write_b32 a9, 0
	v_accvgpr_write_b32 a10, 0
	v_accvgpr_write_b32 a11, 0
	v_accvgpr_write_b32 a12, 0
	v_accvgpr_write_b32 a13, 0
	v_accvgpr_write_b32 a14, 0
	v_accvgpr_write_b32 a15, 0
	v_accvgpr_write_b32 a16, 0
	v_accvgpr_write_b32 a17, 0
	v_accvgpr_write_b32 a18, 0
	v_accvgpr_write_b32 a19, 0
	v_accvgpr_write_b32 a20, 0
	v_accvgpr_write_b32 a21, 0
	v_accvgpr_write_b32 a22, 0
	v_accvgpr_write_b32 a23, 0
	v_accvgpr_write_b32 a24, 0
	v_accvgpr_write_b32 a25, 0
	v_accvgpr_write_b32 a26, 0
	v_accvgpr_write_b32 a27, 0
	v_accvgpr_write_b32 a28, 0
	v_accvgpr_write_b32 a29, 0
	v_accvgpr_write_b32 a30, 0
	v_accvgpr_write_b32 a31, 0
	v_accvgpr_write_b32 a32, 0
	v_accvgpr_write_b32 a33, 0
	v_accvgpr_write_b32 a34, 0
	v_accvgpr_write_b32 a35, 0
	v_accvgpr_write_b32 a36, 0
	v_accvgpr_write_b32 a37, 0
	v_accvgpr_write_b32 a38, 0
	v_accvgpr_write_b32 a39, 0
	v_mov_b32_e32 v2, 0
	v_mov_b32_e32 v3, 0
	v_mov_b32_e32 v4, 0
	v_mov_b32_e32 v5, 0
	v_lshrrev_b32_e32 v44, 1, v46
	v_subrev_u32_e32 v44, s17, v44
	v_and_b32_e32 v44, 63, v44
	v_lshlrev_b32_e32 v44, 5, v44
	v_and_b32_e32 v45, 1, v46
	v_lshl_or_b32 v44, v45, 4, v44
	v_xor_b32_e32 v45, 0x400, v44
	s_mul_i32 s23, s15, 0x1900
	s_add_u32 s23, s23, 75776
	v_add_u32_e32 v44, s23, v44
	v_add_u32_e32 v45, s23, v45
	v_add_u32_e32 v47, s23, v1
	ds_write_b128 v47, v[2:5] offset:4096
	ds_write_b128 v47, v[2:5] offset:5120
	s_waitcnt vmcnt(8)
	ds_write_b128 v44, v[48:51]
	ds_write_b128 v45, v[52:55]
	ds_write_b128 v44, v[56:59] offset:2048
	ds_write_b128 v45, v[60:63] offset:2048
	v_cvt_f16_f32_e32 v42, v42
	v_cvt_f16_f32_e32 v43, v43
	s_mov_b32 s28, 0x5040100
	v_perm_b32 v42, v42, v42, s28
	v_perm_b32 v43, v43, v43, s28
	v_lshrrev_b32_e32 v44, 5, v46
	v_and_b32_e32 v45, 15, v46
	v_bfe_u32 v47, v46, 4, 1
	v_cmp_eq_u32_e32 vcc, v45, v47
	v_lshlrev_b32_e32 v44, 4, v44
	v_add_u32_e32 v46, s23, v44
	v_add_u32_e32 v45, 0x800, v46
	v_mov_b32_e32 v47, s23
	v_add_u32_e32 v47, 0x1000, v47
	v_cndmask_b32_e32 v47, v47, v45, vcc
	s_waitcnt lgkmcnt(0)
	ds_read_b128 v[144:147], v46
	ds_read_b128 v[148:151], v46 offset:32
	ds_read_b128 v[160:163], v47
	ds_read_b128 v[152:155], v46 offset:64
	ds_read_b128 v[164:167], v47 offset:32
	s_add_u32 s27, s17, 8
	s_lshl_b32 s27, s27, 10
	s_add_u32 s29, s17, 63
	s_lshl_b32 s29, s29, 10
	s_movk_i32 s28, 0x400
	s_mov_b32 s26, 0
	s_waitcnt lgkmcnt(4)
	v_pk_max_u16 v128, v144, v42
	v_pk_max_u16 v129, v145, v42
	v_pk_max_u16 v130, v146, v42
	v_pk_max_u16 v131, v147, v42
	v_pk_max_u16 v136, v144, v43
	v_pk_max_u16 v137, v145, v43
	v_pk_max_u16 v138, v146, v43
	v_pk_max_u16 v139, v147, v43
	s_mov_b32 s31, 0xfc00
	s_cmp_ge_u32 s15, 4
	s_cbranch_scc0 .Lk2_noprio
	s_setprio 1
.Lk2_noprio:
.Lk2_loop:
	s_and_b32 s23, s27, s31
	s_add_u32 s24, s20, s23
	s_addc_u32 s25, s21, 0
	s_add_u32 s27, s27, s28
	s_waitcnt vmcnt(7)
	s_waitcnt lgkmcnt(2)
	v_mfma_f32_32x32x16_f16 a[0:15], v[64:67], v[128:131], a[0:15]
	v_pk_max_u16 v132, v148, v42
	v_pk_max_u16 v133, v149, v42
	v_pk_max_u16 v134, v150, v42
	v_pk_max_u16 v135, v151, v42
	v_mfma_f32_32x32x16_f16 a[16:31], v[64:67], v[136:139], a[16:31]
	v_pk_max_u16 v140, v148, v43
	v_pk_max_u16 v141, v149, v43
	v_pk_max_u16 v142, v150, v43
	v_pk_max_u16 v143, v151, v43
	v_mfma_f32_16x16x32_f16 a[32:35], v[160:163], v[128:131], a[32:35]
	global_load_dwordx4 v[64:67], v1, s[24:25]
	ds_read_b128 v[156:159], v46 offset:96
	ds_read_b128 v[168:171], v47 offset:64
	v_mfma_f32_16x16x32_f16 a[36:39], v[160:163], v[136:139], a[36:39]
	s_and_b32 s23, s27, s31
	s_add_u32 s24, s20, s23
	s_addc_u32 s25, s21, 0
	s_add_u32 s27, s27, s28
	s_waitcnt vmcnt(7)
	s_waitcnt lgkmcnt(2)
	v_mfma_f32_32x32x16_f16 a[0:15], v[68:71], v[132:135], a[0:15]
	v_pk_max_u16 v128, v152, v42
	v_pk_max_u16 v129, v153, v42
	v_pk_max_u16 v130, v154, v42
	v_pk_max_u16 v131, v155, v42
	v_mfma_f32_32x32x16_f16 a[16:31], v[68:71], v[140:143], a[16:31]
	v_pk_max_u16 v136, v152, v43
	v_pk_max_u16 v137, v153, v43
	v_pk_max_u16 v138, v154, v43
	v_pk_max_u16 v139, v155, v43
	v_mfma_f32_16x16x32_f16 a[32:35], v[164:167], v[132:135], a[32:35]
	global_load_dwordx4 v[68:71], v1, s[24:25]
	ds_read_b128 v[144:147], v46 offset:128
	ds_read_b128 v[172:175], v47 offset:96
	v_mfma_f32_16x16x32_f16 a[36:39], v[164:167], v[140:143], a[36:39]
	s_and_b32 s23, s27, s31
	s_add_u32 s24, s20, s23
	s_addc_u32 s25, s21, 0
	s_add_u32 s27, s27, s28
	s_waitcnt vmcnt(7)
	s_waitcnt lgkmcnt(2)
	v_mfma_f32_32x32x16_f16 a[0:15], v[72:75], v[128:131], a[0:15]
	v_pk_max_u16 v132, v156, v42
	v_pk_max_u16 v133, v157, v42
	v_pk_max_u16 v134, v158, v42
	v_pk_max_u16 v135, v159, v42
	v_mfma_f32_32x32x16_f16 a[16:31], v[72:75], v[136:139], a[16:31]
	v_pk_max_u16 v140, v156, v43
	v_pk_max_u16 v141, v157, v43
	v_pk_max_u16 v142, v158, v43
	v_pk_max_u16 v143, v159, v43
	v_mfma_f32_16x16x32_f16 a[32:35], v[168:171], v[128:131], a[32:35]
	global_load_dwordx4 v[72:75], v1, s[24:25]
	ds_read_b128 v[148:151], v46 offset:160
	ds_read_b128 v[160:163], v47 offset:128
	v_mfma_f32_16x16x32_f16 a[36:39], v[168:171], v[136:139], a[36:39]
	s_and_b32 s23, s27, s31
	s_add_u32 s24, s20, s23
	s_addc_u32 s25, s21, 0
	s_add_u32 s27, s27, s28
	s_waitcnt vmcnt(7)
	s_waitcnt lgkmcnt(2)
	v_mfma_f32_32x32x16_f16 a[0:15], v[76:79], v[132:135], a[0:15]
	v_pk_max_u16 v128, v144, v42
	v_pk_max_u16 v129, v145, v42
	v_pk_max_u16 v130, v146, v42
	v_pk_max_u16 v131, v147, v42
	v_mfma_f32_32x32x16_f16 a[16:31], v[76:79], v[140:143], a[16:31]
	v_pk_max_u16 v136, v144, v43
	v_pk_max_u16 v137, v145, v43
	v_pk_max_u16 v138, v146, v43
	v_pk_max_u16 v139, v147, v43
	v_mfma_f32_16x16x32_f16 a[32:35], v[172:175], v[132:135], a[32:35]
	global_load_dwordx4 v[76:79], v1, s[24:25]
	ds_read_b128 v[152:155], v46 offset:192
	ds_read_b128 v[164:167], v47 offset:160
	v_mfma_f32_16x16x32_f16 a[36:39], v[172:175], v[140:143], a[36:39]
	s_and_b32 s23, s27, s31
	s_add_u32 s24, s20, s23
	s_addc_u32 s25, s21, 0
	s_add_u32 s27, s27, s28
	s_waitcnt vmcnt(7)
	s_waitcnt lgkmcnt(2)
	v_mfma_f32_32x32x16_f16 a[0:15], v[80:83], v[128:131], a[0:15]
	v_pk_max_u16 v132, v148, v42
	v_pk_max_u16 v133, v149, v42
	v_pk_max_u16 v134, v150, v42
	v_pk_max_u16 v135, v151, v42
	v_mfma_f32_32x32x16_f16 a[16:31], v[80:83], v[136:139], a[16:31]
	v_pk_max_u16 v140, v148, v43
	v_pk_max_u16 v141, v149, v43
	v_pk_max_u16 v142, v150, v43
	v_pk_max_u16 v143, v151, v43
	v_mfma_f32_16x16x32_f16 a[32:35], v[160:163], v[128:131], a[32:35]
	global_load_dwordx4 v[80:83], v1, s[24:25]
	ds_read_b128 v[156:159], v46 offset:224
	ds_read_b128 v[168:171], v47 offset:192
	v_mfma_f32_16x16x32_f16 a[36:39], v[160:163], v[136:139], a[36:39]
	s_and_b32 s23, s27, s31
	s_add_u32 s24, s20, s23
	s_addc_u32 s25, s21, 0
	s_add_u32 s27, s27, s28
	s_waitcnt vmcnt(7)
	s_waitcnt lgkmcnt(2)
	v_mfma_f32_32x32x16_f16 a[0:15], v[84:87], v[132:135], a[0:15]
	v_pk_max_u16 v128, v152, v42
	v_pk_max_u16 v129, v153, v42
	v_pk_max_u16 v130, v154, v42
	v_pk_max_u16 v131, v155, v42
	v_mfma_f32_32x32x16_f16 a[16:31], v[84:87], v[140:143], a[16:31]
	v_pk_max_u16 v136, v152, v43
	v_pk_max_u16 v137, v153, v43
	v_pk_max_u16 v138, v154, v43
	v_pk_max_u16 v139, v155, v43
	v_mfma_f32_16x16x32_f16 a[32:35], v[164:167], v[132:135], a[32:35]
	global_load_dwordx4 v[84:87], v1, s[24:25]
	ds_read_b128 v[144:147], v46 offset:256
	ds_read_b128 v[172:175], v47 offset:224
	v_mfma_f32_16x16x32_f16 a[36:39], v[164:167], v[140:143], a[36:39]
	s_and_b32 s23, s27, s31
	s_add_u32 s24, s20, s23
	s_addc_u32 s25, s21, 0
	s_add_u32 s27, s27, s28
	s_waitcnt vmcnt(7)
	s_waitcnt lgkmcnt(2)
	v_mfma_f32_32x32x16_f16 a[0:15], v[88:91], v[128:131], a[0:15]
	v_pk_max_u16 v132, v156, v42
	v_pk_max_u16 v133, v157, v42
	v_pk_max_u16 v134, v158, v42
	v_pk_max_u16 v135, v159, v42
	v_mfma_f32_32x32x16_f16 a[16:31], v[88:91], v[136:139], a[16:31]
	v_pk_max_u16 v140, v156, v43
	v_pk_max_u16 v141, v157, v43
	v_pk_max_u16 v142, v158, v43
	v_pk_max_u16 v143, v159, v43
	v_mfma_f32_16x16x32_f16 a[32:35], v[168:171], v[128:131], a[32:35]
	global_load_dwordx4 v[88:91], v1, s[24:25]
	ds_read_b128 v[148:151], v46 offset:288
	ds_read_b128 v[160:163], v47 offset:256
	v_mfma_f32_16x16x32_f16 a[36:39], v[168:171], v[136:139], a[36:39]
	s_and_b32 s23, s27, s31
	s_add_u32 s24, s20, s23
	s_addc_u32 s25, s21, 0
	s_add_u32 s27, s27, s28
	s_waitcnt vmcnt(7)
	s_waitcnt lgkmcnt(2)
	v_mfma_f32_32x32x16_f16 a[0:15], v[92:95], v[132:135], a[0:15]
	v_pk_max_u16 v128, v144, v42
	v_pk_max_u16 v129, v145, v42
	v_pk_max_u16 v130, v146, v42
	v_pk_max_u16 v131, v147, v42
	v_mfma_f32_32x32x16_f16 a[16:31], v[92:95], v[140:143], a[16:31]
	v_pk_max_u16 v136, v144, v43
	v_pk_max_u16 v137, v145, v43
	v_pk_max_u16 v138, v146, v43
	v_pk_max_u16 v139, v147, v43
	v_mfma_f32_16x16x32_f16 a[32:35], v[172:175], v[132:135], a[32:35]
	global_load_dwordx4 v[92:95], v1, s[24:25]
	ds_read_b128 v[152:155], v46 offset:320
	ds_read_b128 v[164:167], v47 offset:288
	v_mfma_f32_16x16x32_f16 a[36:39], v[172:175], v[140:143], a[36:39]
	s_add_u32 s26, s26, 1
	v_add_u32_e32 v46, 256, v46
	v_add_u32_e32 v47, 256, v47
	s_cmp_eq_u32 s26, 7
	s_cselect_b32 s27, s29, s27
	s_cselect_b32 s28, 0, s28
	s_cmp_lt_u32 s26, 8
	s_cbranch_scc1 .Lk2_loop
	v_and_b32_e32 v2, 63, v0
	v_lshrrev_b32_e32 v3, 5, v2
	v_and_b32_e32 v4, 31, v0
	s_lshl_b32 s23, s15, 4
	v_add_u32_e32 v3, s23, v3
	v_mul_u32_u24_e32 v3, 576, v3
	v_lshl_add_u32 v3, v4, 4, v3
	v_cmp_gt_u32_e32 vcc, 16, v2
	ds_write_b128 v3, a[0:3]
	ds_write_b128 v3, a[16:19] offset:4608
	ds_write_b128 v3, a[4:7] offset:1152
	ds_write_b128 v3, a[20:23] offset:5760
	ds_write_b128 v3, a[8:11] offset:2304
	ds_write_b128 v3, a[24:27] offset:6912
	ds_write_b128 v3, a[12:15] offset:3456
	ds_write_b128 v3, a[28:31] offset:8064
	s_and_saveexec_b64 s[2:3], vcc
	s_cbranch_execz .Lk2_nodred
	v_lshlrev_b32_e32 v5, 2, v2
	s_lshl_b32 s23, s15, 8
	v_add_u32_e32 v5, s23, v5
	v_add_u32_e32 v5, 73728, v5
	ds_write2_b32 v5, a32, a33 offset1:16
	ds_write2_b32 v5, a36, a37 offset0:32 offset1:48
.Lk2_nodred:
	s_or_b64 exec, exec, s[2:3]
	v_lshrrev_b32_e32 v6, 3, v0
	v_and_b32_e32 v7, 7, v0
	v_lshrrev_b32_e32 v8, 8, v0
	v_bfe_u32 v9, v0, 3, 5
	v_lshlrev_b32_e32 v10, 2, v9
	v_lshl_or_b32 v10, v8, 7, v10
	v_add_u32_e32 v10, 73728, v10
	v_mul_u32_u24_e32 v11, 4608, v8
	v_mul_u32_u24_e32 v12, 576, v7
	v_lshlrev_b32_e32 v13, 4, v9
	v_add3_u32 v11, v11, v12, v13
	s_lshl_b32 s4, s18, 6
	v_or_b32_e32 v14, s4, v6
	v_mov_b32_e32 v15, 0
	v_lshlrev_b64 v[16:17], 8, v[14:15]
	v_lshl_add_u64 v[16:17], s[12:13], 0, v[16:17]
	s_lshl_b32 s2, s16, 7
	s_mov_b32 s3, 0
	v_lshl_add_u64 v[16:17], v[16:17], 0, s[2:3]
	v_lshlrev_b32_e32 v14, 4, v7
	v_lshl_add_u64 v[16:17], v[16:17], 0, v[14:15]
	s_waitcnt lgkmcnt(0)
	s_barrier
	ds_read_b32 v50, v10
	ds_read_b32 v51, v10 offset:256
	ds_read_b32 v52, v10 offset:512
	ds_read_b32 v53, v10 offset:768
	ds_read_b32 v54, v10 offset:1024
	ds_read_b32 v55, v10 offset:1280
	ds_read_b32 v56, v10 offset:1536
	ds_read_b32 v57, v10 offset:1792
	ds_read_b128 v[18:21], v11
	ds_read_b128 v[22:25], v11 offset:9216
	ds_read_b128 v[26:29], v11 offset:18432
	ds_read_b128 v[30:33], v11 offset:27648
	ds_read_b128 v[34:37], v11 offset:36864
	ds_read_b128 v[38:41], v11 offset:46080
	ds_read_b128 v[42:45], v11 offset:55296
	s_waitcnt lgkmcnt(13)
	ds_read_b128 v[46:49], v11 offset:64512
	v_add_f32_e32 v2, v50, v51
	s_waitcnt lgkmcnt(13)
	v_add_f32_e32 v2, v2, v52
	s_waitcnt lgkmcnt(12)
	v_add_f32_e32 v2, v2, v53
	s_waitcnt lgkmcnt(11)
	v_add_f32_e32 v2, v2, v54
	s_waitcnt lgkmcnt(10)
	v_add_f32_e32 v2, v2, v55
	s_waitcnt lgkmcnt(9)
	v_add_f32_e32 v2, v2, v56
	s_waitcnt lgkmcnt(8)
	v_add_f32_e32 v2, v2, v57
	v_div_scale_f32 v3, s[2:3], v2, v2, 1.0
	v_rcp_f32_e32 v4, v3
	v_div_scale_f32 v5, vcc, 1.0, v2, 1.0
	v_fma_f32 v6, -v3, v4, 1.0
	v_fmac_f32_e32 v4, v6, v4
	v_mul_f32_e32 v6, v5, v4
	v_fma_f32 v7, -v3, v6, v5
	v_fmac_f32_e32 v6, v7, v4
	v_fma_f32 v3, -v3, v6, v5
	v_div_fmas_f32 v3, v3, v4, v6
	v_div_fixup_f32 v8, v3, v2, 1.0
	s_waitcnt lgkmcnt(6)
	v_pk_add_f32 v[60:61], v[20:21], v[24:25]
	v_pk_add_f32 v[58:59], v[18:19], v[22:23]
	s_waitcnt lgkmcnt(5)
	v_pk_add_f32 v[60:61], v[60:61], v[28:29]
	v_pk_add_f32 v[58:59], v[58:59], v[26:27]
	s_waitcnt lgkmcnt(4)
	v_pk_add_f32 v[60:61], v[60:61], v[32:33]
	v_pk_add_f32 v[58:59], v[58:59], v[30:31]
	s_waitcnt lgkmcnt(3)
	v_pk_add_f32 v[60:61], v[60:61], v[36:37]
	v_pk_add_f32 v[58:59], v[58:59], v[34:35]
	s_waitcnt lgkmcnt(2)
	v_pk_add_f32 v[60:61], v[60:61], v[40:41]
	v_pk_add_f32 v[58:59], v[58:59], v[38:39]
	s_waitcnt lgkmcnt(1)
	v_pk_add_f32 v[60:61], v[60:61], v[44:45]
	v_pk_add_f32 v[58:59], v[58:59], v[42:43]
	s_waitcnt lgkmcnt(0)
	v_pk_add_f32 v[60:61], v[60:61], v[48:49]
	v_pk_add_f32 v[58:59], v[58:59], v[46:47]
	v_pk_mul_f32 v[60:61], v[60:61], v[8:9] op_sel_hi:[1,0]
	v_pk_mul_f32 v[58:59], v[58:59], v[8:9] op_sel_hi:[1,0]
	global_store_dwordx4 v[16:17], v[58:61], off sc1
	s_endpgm

	.amdhsa_kernel _Z6gat_k2PKDF16_S0_S0_PKfPf
		.amdhsa_group_segment_fixed_size 126976
		.amdhsa_private_segment_fixed_size 0
		.amdhsa_kernarg_size 40
		.amdhsa_user_sgpr_count 2
		.amdhsa_user_sgpr_dispatch_ptr 0
		.amdhsa_user_sgpr_queue_ptr 0
		.amdhsa_user_sgpr_kernarg_segment_ptr 1
		.amdhsa_user_sgpr_dispatch_id 0
		.amdhsa_user_sgpr_kernarg_preload_length 0
		.amdhsa_user_sgpr_kernarg_preload_offset 0
		.amdhsa_user_sgpr_private_segment_size 0
		.amdhsa_uses_dynamic_stack 0
		.amdhsa_enable_private_segment 0
		.amdhsa_system_sgpr_workgroup_id_x 1
		.amdhsa_system_sgpr_workgroup_id_y 0
		.amdhsa_system_sgpr_workgroup_id_z 0
		.amdhsa_system_sgpr_workgroup_info 0
		.amdhsa_system_vgpr_workitem_id 0
		.amdhsa_next_free_vgpr 216
		.amdhsa_next_free_sgpr 96
		.amdhsa_accum_offset 176
		.amdhsa_reserve_vcc 1
		.amdhsa_float_round_mode_32 0
		.amdhsa_float_round_mode_16_64 0
		.amdhsa_float_denorm_mode_32 3
		.amdhsa_float_denorm_mode_16_64 3
		.amdhsa_dx10_clamp 1
		.amdhsa_ieee_mode 1
		.amdhsa_fp16_overflow 0
		.amdhsa_tg_split 0
		.amdhsa_exception_fp_ieee_invalid_op 0
		.amdhsa_exception_fp_denorm_src 0
		.amdhsa_exception_fp_ieee_div_zero 0
		.amdhsa_exception_fp_ieee_overflow 0
		.amdhsa_exception_fp_ieee_underflow 0
		.amdhsa_exception_fp_ieee_inexact 0
		.amdhsa_exception_int_div_zero 0
	.end_amdhsa_kernel

amdhsa.kernels:
  - .agpr_count:     32
    .args:
      - .actual_access:  read_only
        .address_space:  global
        .offset:         0
        .size:           8
        .value_kind:     global_buffer
      - .actual_access:  read_only
        .address_space:  global
        .offset:         8
        .size:           8
        .value_kind:     global_buffer
      - .actual_access:  read_only
        .address_space:  global
        .offset:         16
        .size:           8
        .value_kind:     global_buffer
      - .actual_access:  read_only
        .address_space:  global
        .offset:         24
        .size:           8
        .value_kind:     global_buffer
      - .actual_access:  write_only
        .address_space:  global
        .offset:         32
        .size:           8
        .value_kind:     global_buffer
      - .actual_access:  write_only
        .address_space:  global
        .offset:         40
        .size:           8
        .value_kind:     global_buffer
      - .actual_access:  write_only
        .address_space:  global
        .offset:         48
        .size:           8
        .value_kind:     global_buffer
      - .actual_access:  write_only
        .address_space:  global
        .offset:         56
        .size:           8
        .value_kind:     global_buffer
    .group_segment_fixed_size: 68352
    .kernarg_segment_align: 8
    .kernarg_segment_size: 64
    .language:       OpenCL C
    .language_version:
      - 2
      - 0
    .max_flat_workgroup_size: 256
    .name:           _Z6gat_k1PKfS0_S0_S0_PDF16_S1_S1_Pf
    .private_segment_fixed_size: 0
    .sgpr_count:     26
    .sgpr_spill_count: 0
    .symbol:         _Z6gat_k1PKfS0_S0_S0_PDF16_S1_S1_Pf.kd
    .uniform_work_group_size: 1
    .uses_dynamic_stack: false
    .vgpr_count:     156
    .vgpr_spill_count: 0
    .wavefront_size: 64
  - .agpr_count:     40
    .args:
      - .actual_access:  read_only
        .address_space:  global
        .offset:         0
        .size:           8
        .value_kind:     global_buffer
      - .actual_access:  read_only
        .address_space:  global
        .offset:         8
        .size:           8
        .value_kind:     global_buffer
      - .actual_access:  read_only
        .address_space:  global
        .offset:         16
        .size:           8
        .value_kind:     global_buffer
      - .actual_access:  read_only
        .address_space:  global
        .offset:         24
        .size:           8
        .value_kind:     global_buffer
      - .actual_access:  write_only
        .address_space:  global
        .offset:         32
        .size:           8
        .value_kind:     global_buffer
    .group_segment_fixed_size: 126976
    .kernarg_segment_align: 8
    .kernarg_segment_size: 40
    .language:       OpenCL C
    .language_version:
      - 2
      - 0
    .max_flat_workgroup_size: 512
    .name:           _Z6gat_k2PKDF16_S0_S0_PKfPf
    .private_segment_fixed_size: 0
    .sgpr_count:     38
    .sgpr_spill_count: 0
    .symbol:         _Z6gat_k2PKDF16_S0_S0_PKfPf.kd
    .uniform_work_group_size: 1
    .uses_dynamic_stack: false
    .vgpr_count:     216
    .vgpr_spill_count: 0
    .wavefront_size: 64
